# GEMM K-loops: M0-write to LDS-DMA wait states filled by a ds_read of the same phase instead of s_nop (22 sites)
# baseline (speedup 1.0000x reference)
.LBB3_34:
	s_mov_b32 m0, s66
	ds_read_b128 v[98:101], v94 offset:16384
	ds_read_b128 v[102:105], v94 offset:17408
	ds_read_b128 v[106:109], v94 offset:18432
	ds_read_b128 v[110:113], v94 offset:19456
	ds_read_b128 v[114:117], v95
	ds_read_b128 v[118:121], v95 offset:1024
	ds_read_b128 v[122:125], v95 offset:2048
	ds_read_b128 v[126:129], v95 offset:3072
	ds_read_b128 v[130:133], v95 offset:4096
	ds_read_b128 v[134:137], v95 offset:5120
	ds_read_b128 v[138:141], v95 offset:6144
	global_load_lds_dwordx4 v60, s[68:69]
	s_add_i32 m0, s66, 0x2000
	ds_read_b128 v[142:145], v95 offset:7168
	global_load_lds_dwordx4 v62, s[68:69]
	s_barrier
	s_setprio 1
	s_waitcnt lgkmcnt(7)
	v_mfma_f32_16x16x32_f16 v[44:47], v[98:101], v[114:117], v[44:47]
	v_mfma_f32_16x16x32_f16 v[40:43], v[106:109], v[114:117], v[40:43]
	s_waitcnt lgkmcnt(5)
	v_mfma_f32_16x16x32_f16 v[32:35], v[98:101], v[122:125], v[32:35]
	v_mfma_f32_16x16x32_f16 v[28:31], v[106:109], v[122:125], v[28:31]
	s_waitcnt lgkmcnt(3)
	v_mfma_f32_16x16x32_f16 v[20:23], v[98:101], v[130:133], v[20:23]
	v_mfma_f32_16x16x32_f16 v[16:19], v[106:109], v[130:133], v[16:19]
	s_waitcnt lgkmcnt(1)
	v_mfma_f32_16x16x32_f16 v[8:11], v[98:101], v[138:141], v[8:11]
	v_mfma_f32_16x16x32_f16 v[4:7], v[106:109], v[138:141], v[4:7]
	v_mfma_f32_16x16x32_f16 v[44:47], v[102:105], v[118:121], v[44:47]
	v_mfma_f32_16x16x32_f16 v[40:43], v[110:113], v[118:121], v[40:43]
	v_mfma_f32_16x16x32_f16 v[32:35], v[102:105], v[126:129], v[32:35]
	v_mfma_f32_16x16x32_f16 v[28:31], v[110:113], v[126:129], v[28:31]
	v_mfma_f32_16x16x32_f16 v[20:23], v[102:105], v[134:137], v[20:23]
	v_mfma_f32_16x16x32_f16 v[16:19], v[110:113], v[134:137], v[16:19]
	s_waitcnt lgkmcnt(0)
	v_mfma_f32_16x16x32_f16 v[8:11], v[102:105], v[142:145], v[8:11]
	v_mfma_f32_16x16x32_f16 v[4:7], v[110:113], v[142:145], v[4:7]
	s_setprio 0
	s_barrier
	s_add_i32 m0, s43, 0x18000
	ds_read_b128 v[98:101], v94 offset:20480
	global_load_lds_dwordx4 v64, s[70:71]
	s_add_i32 m0, s43, 0x1a000
	ds_read_b128 v[102:105], v94 offset:21504
	global_load_lds_dwordx4 v66, s[70:71]
	s_add_i32 m0, s43, 0x1c000
	s_nop 0
	global_load_lds_dwordx4 v68, s[70:71]
	s_waitcnt vmcnt(5)
	s_barrier
	s_setprio 1
	s_waitcnt lgkmcnt(1)
	v_mfma_f32_16x16x32_f16 v[36:39], v[98:101], v[114:117], v[36:39]
	v_mfma_f32_16x16x32_f16 v[24:27], v[98:101], v[122:125], v[24:27]
	v_mfma_f32_16x16x32_f16 v[12:15], v[98:101], v[130:133], v[12:15]
	v_mfma_f32_16x16x32_f16 v[0:3], v[98:101], v[138:141], v[0:3]
	s_waitcnt lgkmcnt(0)
	v_mfma_f32_16x16x32_f16 v[36:39], v[102:105], v[118:121], v[36:39]
	v_mfma_f32_16x16x32_f16 v[24:27], v[102:105], v[126:129], v[24:27]
	v_mfma_f32_16x16x32_f16 v[12:15], v[102:105], v[134:137], v[12:15]
	v_mfma_f32_16x16x32_f16 v[0:3], v[102:105], v[142:145], v[0:3]
	s_setprio 0
	s_barrier
	s_mov_b32 m0, s43
	ds_read_b128 v[98:101], v94 offset:57344
	ds_read_b128 v[102:105], v94 offset:58368
	ds_read_b128 v[106:109], v94 offset:59392
	ds_read_b128 v[110:113], v94 offset:60416
	ds_read_b128 v[114:117], v95 offset:40960
	ds_read_b128 v[118:121], v95 offset:41984
	ds_read_b128 v[122:125], v95 offset:43008
	ds_read_b128 v[126:129], v95 offset:44032
	ds_read_b128 v[130:133], v95 offset:45056
	ds_read_b128 v[134:137], v95 offset:46080
	ds_read_b128 v[138:141], v95 offset:47104
	global_load_lds_dwordx4 v48, s[64:65]
	s_mov_b32 m0, s44
	ds_read_b128 v[142:145], v95 offset:48128
	global_load_lds_dwordx4 v52, s[64:65]
	s_barrier
	s_setprio 1
	s_waitcnt lgkmcnt(7)
	v_mfma_f32_16x16x32_f16 v[44:47], v[98:101], v[114:117], v[44:47]
	v_mfma_f32_16x16x32_f16 v[40:43], v[106:109], v[114:117], v[40:43]
	s_waitcnt lgkmcnt(5)
	v_mfma_f32_16x16x32_f16 v[32:35], v[98:101], v[122:125], v[32:35]
	v_mfma_f32_16x16x32_f16 v[28:31], v[106:109], v[122:125], v[28:31]
	s_waitcnt lgkmcnt(3)
	v_mfma_f32_16x16x32_f16 v[20:23], v[98:101], v[130:133], v[20:23]
	v_mfma_f32_16x16x32_f16 v[16:19], v[106:109], v[130:133], v[16:19]
	s_waitcnt lgkmcnt(1)
	v_mfma_f32_16x16x32_f16 v[8:11], v[98:101], v[138:141], v[8:11]
	v_mfma_f32_16x16x32_f16 v[4:7], v[106:109], v[138:141], v[4:7]
	v_mfma_f32_16x16x32_f16 v[44:47], v[102:105], v[118:121], v[44:47]
	v_mfma_f32_16x16x32_f16 v[40:43], v[110:113], v[118:121], v[40:43]
	v_mfma_f32_16x16x32_f16 v[32:35], v[102:105], v[126:129], v[32:35]
	v_mfma_f32_16x16x32_f16 v[28:31], v[110:113], v[126:129], v[28:31]
	v_mfma_f32_16x16x32_f16 v[20:23], v[102:105], v[134:137], v[20:23]
	v_mfma_f32_16x16x32_f16 v[16:19], v[110:113], v[134:137], v[16:19]
	s_waitcnt lgkmcnt(0)
	v_mfma_f32_16x16x32_f16 v[8:11], v[102:105], v[142:145], v[8:11]
	v_mfma_f32_16x16x32_f16 v[4:7], v[110:113], v[142:145], v[4:7]
	s_setprio 0
	s_barrier
	s_mov_b32 m0, s45
	ds_read_b128 v[98:101], v94 offset:61440
	global_load_lds_dwordx4 v50, s[26:27]
	s_mov_b32 m0, s46
	ds_read_b128 v[102:105], v94 offset:62464
	global_load_lds_dwordx4 v54, s[26:27]
	s_mov_b32 m0, s47
	s_nop 0
	global_load_lds_dwordx4 v56, s[26:27]
	s_waitcnt vmcnt(5)
	s_barrier
	s_setprio 1
	s_waitcnt lgkmcnt(1)
	v_mfma_f32_16x16x32_f16 v[36:39], v[98:101], v[114:117], v[36:39]
	v_mfma_f32_16x16x32_f16 v[24:27], v[98:101], v[122:125], v[24:27]
	v_mfma_f32_16x16x32_f16 v[12:15], v[98:101], v[130:133], v[12:15]
	v_mfma_f32_16x16x32_f16 v[0:3], v[98:101], v[138:141], v[0:3]
	s_waitcnt lgkmcnt(0)
	v_mfma_f32_16x16x32_f16 v[36:39], v[102:105], v[118:121], v[36:39]
	v_mfma_f32_16x16x32_f16 v[24:27], v[102:105], v[126:129], v[24:27]
	v_mfma_f32_16x16x32_f16 v[12:15], v[102:105], v[134:137], v[12:15]
	v_mfma_f32_16x16x32_f16 v[0:3], v[102:105], v[142:145], v[0:3]
	s_setprio 0
	s_barrier
	s_mov_b32 m0, s52
	ds_read_b128 v[98:101], v96
	ds_read_b128 v[102:105], v96 offset:1024
	ds_read_b128 v[106:109], v96 offset:2048
	ds_read_b128 v[110:113], v96 offset:3072
	ds_read_b128 v[114:117], v97
	ds_read_b128 v[118:121], v97 offset:1024
	ds_read_b128 v[122:125], v97 offset:2048
	ds_read_b128 v[126:129], v97 offset:3072
	ds_read_b128 v[130:133], v97 offset:4096
	ds_read_b128 v[134:137], v97 offset:5120
	ds_read_b128 v[138:141], v97 offset:6144
	global_load_lds_dwordx4 v48, s[72:73]
	s_mov_b32 m0, s53
	ds_read_b128 v[142:145], v97 offset:7168
	global_load_lds_dwordx4 v52, s[72:73]
	s_barrier
	s_setprio 1
	s_waitcnt lgkmcnt(7)
	v_mfma_f32_16x16x32_f16 v[44:47], v[98:101], v[114:117], v[44:47]
	v_mfma_f32_16x16x32_f16 v[40:43], v[106:109], v[114:117], v[40:43]
	s_waitcnt lgkmcnt(5)
	v_mfma_f32_16x16x32_f16 v[32:35], v[98:101], v[122:125], v[32:35]
	v_mfma_f32_16x16x32_f16 v[28:31], v[106:109], v[122:125], v[28:31]
	s_waitcnt lgkmcnt(3)
	v_mfma_f32_16x16x32_f16 v[20:23], v[98:101], v[130:133], v[20:23]
	v_mfma_f32_16x16x32_f16 v[16:19], v[106:109], v[130:133], v[16:19]
	s_waitcnt lgkmcnt(1)
	v_mfma_f32_16x16x32_f16 v[8:11], v[98:101], v[138:141], v[8:11]
	v_mfma_f32_16x16x32_f16 v[4:7], v[106:109], v[138:141], v[4:7]
	v_mfma_f32_16x16x32_f16 v[44:47], v[102:105], v[118:121], v[44:47]
	v_mfma_f32_16x16x32_f16 v[40:43], v[110:113], v[118:121], v[40:43]
	v_mfma_f32_16x16x32_f16 v[32:35], v[102:105], v[126:129], v[32:35]
	v_mfma_f32_16x16x32_f16 v[28:31], v[110:113], v[126:129], v[28:31]
	v_mfma_f32_16x16x32_f16 v[20:23], v[102:105], v[134:137], v[20:23]
	v_mfma_f32_16x16x32_f16 v[16:19], v[110:113], v[134:137], v[16:19]
	s_waitcnt lgkmcnt(0)
	v_mfma_f32_16x16x32_f16 v[8:11], v[102:105], v[142:145], v[8:11]
	v_mfma_f32_16x16x32_f16 v[4:7], v[110:113], v[142:145], v[4:7]
	s_setprio 0
	s_barrier
	s_mov_b32 m0, s54
	ds_read_b128 v[98:101], v96 offset:4096
	global_load_lds_dwordx4 v50, s[74:75]
	s_add_i32 m0, s54, 0x2000
	ds_read_b128 v[102:105], v96 offset:5120
	global_load_lds_dwordx4 v54, s[74:75]
	s_add_i32 m0, s54, 0x4000
	s_nop 0
	global_load_lds_dwordx4 v56, s[74:75]
	s_waitcnt vmcnt(5)
	s_barrier
	s_setprio 1
	s_waitcnt lgkmcnt(1)
	v_mfma_f32_16x16x32_f16 v[36:39], v[98:101], v[114:117], v[36:39]
	v_mfma_f32_16x16x32_f16 v[24:27], v[98:101], v[122:125], v[24:27]
	v_mfma_f32_16x16x32_f16 v[12:15], v[98:101], v[130:133], v[12:15]
	v_mfma_f32_16x16x32_f16 v[0:3], v[98:101], v[138:141], v[0:3]
	s_waitcnt lgkmcnt(0)
	v_mfma_f32_16x16x32_f16 v[36:39], v[102:105], v[118:121], v[36:39]
	v_mfma_f32_16x16x32_f16 v[24:27], v[102:105], v[126:129], v[24:27]
	v_mfma_f32_16x16x32_f16 v[12:15], v[102:105], v[134:137], v[12:15]
	v_mfma_f32_16x16x32_f16 v[0:3], v[102:105], v[142:145], v[0:3]
	s_setprio 0
	s_add_i32 s63, s63, 3
	s_add_u32 s24, s24, 0x180
	s_addc_u32 s25, s25, 0
	s_cmp_ge_i32 s63, s49
	s_cbranch_scc1 .Lrot_exit_qkv
	s_add_u32 s68, s20, s24
	s_addc_u32 s69, s21, s25
	s_add_u32 s70, s22, s24
	s_addc_u32 s71, s23, s25
	s_add_u32 s26, s20, s24
	s_addc_u32 s27, s21, s25
	s_add_u32 s26, s26, 0x180
	s_addc_u32 s27, s27, 0
	s_add_u32 s64, s22, s24
	s_addc_u32 s65, s23, s25
	s_add_u32 s66, s64, 0x180
	s_addc_u32 s67, s65, 0
	s_cmp_eq_u32 s56, s63
	s_cselect_b32 s65, s5, s27
	s_cselect_b32 s64, s4, s26
	s_cselect_b32 s27, s7, s67
	s_cselect_b32 s26, s6, s66
	s_add_u32 s72, s64, 0x80
	s_addc_u32 s73, s65, 0
	s_add_u32 s74, s26, 0x80
	s_addc_u32 s75, s27, 0
	s_add_i32 s66, s58, s38
	s_barrier
	s_branch .LBB3_34

.LBB4_22:
	s_mov_b32 m0, s70
	ds_read_b128 v[130:133], v136 offset:16384
	ds_read_b128 v[142:145], v136 offset:17408
	ds_read_b128 v[146:149], v136 offset:18432
	ds_read_b128 v[150:153], v136 offset:19456
	ds_read_b128 v[154:157], v137
	ds_read_b128 v[158:161], v137 offset:1024
	ds_read_b128 v[162:165], v137 offset:2048
	ds_read_b128 v[166:169], v137 offset:3072
	ds_read_b128 v[170:173], v137 offset:4096
	ds_read_b128 v[174:177], v137 offset:5120
	ds_read_b128 v[178:181], v137 offset:6144
	global_load_lds_dwordx4 v0, s[74:75]
	s_add_i32 m0, s70, 0x2000
	ds_read_b128 v[182:185], v137 offset:7168
	global_load_lds_dwordx4 v120, s[74:75]
	s_barrier
	s_setprio 1
	s_waitcnt lgkmcnt(7)
	v_mfma_f32_16x16x32_f16 v[94:97], v[130:133], v[154:157], v[94:97]
	v_mfma_f32_16x16x32_f16 v[90:93], v[146:149], v[154:157], v[90:93]
	s_waitcnt lgkmcnt(5)
	v_mfma_f32_16x16x32_f16 v[82:85], v[130:133], v[162:165], v[82:85]
	v_mfma_f32_16x16x32_f16 v[78:81], v[146:149], v[162:165], v[78:81]
	s_waitcnt lgkmcnt(3)
	v_mfma_f32_16x16x32_f16 v[70:73], v[130:133], v[170:173], v[70:73]
	v_mfma_f32_16x16x32_f16 v[66:69], v[146:149], v[170:173], v[66:69]
	s_waitcnt lgkmcnt(1)
	v_mfma_f32_16x16x32_f16 v[58:61], v[130:133], v[178:181], v[58:61]
	v_mfma_f32_16x16x32_f16 v[54:57], v[146:149], v[178:181], v[54:57]
	v_mfma_f32_16x16x32_f16 v[94:97], v[142:145], v[158:161], v[94:97]
	v_mfma_f32_16x16x32_f16 v[90:93], v[150:153], v[158:161], v[90:93]
	v_mfma_f32_16x16x32_f16 v[82:85], v[142:145], v[166:169], v[82:85]
	v_mfma_f32_16x16x32_f16 v[78:81], v[150:153], v[166:169], v[78:81]
	v_mfma_f32_16x16x32_f16 v[70:73], v[142:145], v[174:177], v[70:73]
	v_mfma_f32_16x16x32_f16 v[66:69], v[150:153], v[174:177], v[66:69]
	s_waitcnt lgkmcnt(0)
	v_mfma_f32_16x16x32_f16 v[58:61], v[142:145], v[182:185], v[58:61]
	v_mfma_f32_16x16x32_f16 v[54:57], v[150:153], v[182:185], v[54:57]
	s_setprio 0
	s_barrier
	s_add_i32 m0, s49, 0x18000
	ds_read_b128 v[130:133], v136 offset:20480
	global_load_lds_dwordx4 v122, s[76:77]
	s_add_i32 m0, s49, 0x1a000
	ds_read_b128 v[142:145], v136 offset:21504
	global_load_lds_dwordx4 v124, s[76:77]
	s_add_i32 m0, s49, 0x1c000
	s_nop 0
	global_load_lds_dwordx4 v126, s[76:77]
	s_cmp_lg_u32 s67, 0
	s_cbranch_scc1 .Lpj_norm_0
	s_mul_i32 s72, s66, 0xc0
	v_add_u32_e32 v214, s72, v135
	v_ashrrev_i32_e32 v215, 31, v214
	v_lshl_add_u64 v[214:215], v[214:215], 2, s[10:11]
	global_load_dwordx4 v[202:205], v[214:215], off
	global_load_dwordx4 v[206:209], v[214:215], off offset:64
	global_load_dwordx4 v[210:213], v[214:215], off offset:128
	global_load_dwordx4 v[2:5], v[194:195], off
	global_load_dwordx4 v[6:9], v[194:195], off offset:64
	global_load_dwordx4 v[10:13], v[194:195], off offset:128
	global_load_dwordx4 v[14:17], v[196:197], off
	s_waitcnt vmcnt(12)
	s_branch .Lpj_join_0

.Lpj_join_0:
	s_barrier
	s_setprio 1
	s_waitcnt lgkmcnt(1)
	v_mfma_f32_16x16x32_f16 v[86:89], v[130:133], v[154:157], v[86:89]
	v_mfma_f32_16x16x32_f16 v[74:77], v[130:133], v[162:165], v[74:77]
	v_mfma_f32_16x16x32_f16 v[62:65], v[130:133], v[170:173], v[62:65]
	v_mfma_f32_16x16x32_f16 v[50:53], v[130:133], v[178:181], v[50:53]
	s_waitcnt lgkmcnt(0)
	v_mfma_f32_16x16x32_f16 v[86:89], v[142:145], v[158:161], v[86:89]
	v_mfma_f32_16x16x32_f16 v[74:77], v[142:145], v[166:169], v[74:77]
	v_mfma_f32_16x16x32_f16 v[62:65], v[142:145], v[174:177], v[62:65]
	v_mfma_f32_16x16x32_f16 v[50:53], v[142:145], v[182:185], v[50:53]
	s_setprio 0
	s_barrier
	s_mov_b32 m0, s49
	ds_read_b128 v[130:133], v136 offset:57344
	ds_read_b128 v[142:145], v136 offset:58368
	ds_read_b128 v[146:149], v136 offset:59392
	ds_read_b128 v[150:153], v136 offset:60416
	ds_read_b128 v[154:157], v137 offset:40960
	ds_read_b128 v[158:161], v137 offset:41984
	ds_read_b128 v[162:165], v137 offset:43008
	ds_read_b128 v[166:169], v137 offset:44032
	ds_read_b128 v[170:173], v137 offset:45056
	ds_read_b128 v[174:177], v137 offset:46080
	ds_read_b128 v[178:181], v137 offset:47104
	global_load_lds_dwordx4 v110, s[68:69]
	s_mov_b32 m0, s50
	ds_read_b128 v[182:185], v137 offset:48128
	global_load_lds_dwordx4 v114, s[68:69]
	s_barrier
	s_setprio 1
	s_waitcnt lgkmcnt(7)
	v_mfma_f32_16x16x32_f16 v[94:97], v[130:133], v[154:157], v[94:97]
	v_mfma_f32_16x16x32_f16 v[90:93], v[146:149], v[154:157], v[90:93]
	s_waitcnt lgkmcnt(5)
	v_mfma_f32_16x16x32_f16 v[82:85], v[130:133], v[162:165], v[82:85]
	v_mfma_f32_16x16x32_f16 v[78:81], v[146:149], v[162:165], v[78:81]
	s_waitcnt lgkmcnt(3)
	v_mfma_f32_16x16x32_f16 v[70:73], v[130:133], v[170:173], v[70:73]
	v_mfma_f32_16x16x32_f16 v[66:69], v[146:149], v[170:173], v[66:69]
	s_waitcnt lgkmcnt(1)
	v_mfma_f32_16x16x32_f16 v[58:61], v[130:133], v[178:181], v[58:61]
	v_mfma_f32_16x16x32_f16 v[54:57], v[146:149], v[178:181], v[54:57]
	v_mfma_f32_16x16x32_f16 v[94:97], v[142:145], v[158:161], v[94:97]
	v_mfma_f32_16x16x32_f16 v[90:93], v[150:153], v[158:161], v[90:93]
	v_mfma_f32_16x16x32_f16 v[82:85], v[142:145], v[166:169], v[82:85]
	v_mfma_f32_16x16x32_f16 v[78:81], v[150:153], v[166:169], v[78:81]
	v_mfma_f32_16x16x32_f16 v[70:73], v[142:145], v[174:177], v[70:73]
	v_mfma_f32_16x16x32_f16 v[66:69], v[150:153], v[174:177], v[66:69]
	s_waitcnt lgkmcnt(0)
	v_mfma_f32_16x16x32_f16 v[58:61], v[142:145], v[182:185], v[58:61]
	v_mfma_f32_16x16x32_f16 v[54:57], v[150:153], v[182:185], v[54:57]
	s_setprio 0
	s_barrier
	s_mov_b32 m0, s51
	ds_read_b128 v[130:133], v136 offset:61440
	global_load_lds_dwordx4 v112, s[34:35]
	s_mov_b32 m0, s52
	ds_read_b128 v[142:145], v136 offset:62464
	global_load_lds_dwordx4 v116, s[34:35]
	s_mov_b32 m0, s53
	s_nop 0
	global_load_lds_dwordx4 v118, s[34:35]
	s_cmp_lg_u32 s67, 0
	s_cbranch_scc1 .Lpj_norm_1
	global_load_dwordx4 v[18:21], v[196:197], off offset:64
	global_load_dwordx4 v[22:25], v[196:197], off offset:128
	global_load_dwordx4 v[26:29], v[198:199], off
	global_load_dwordx4 v[30:33], v[198:199], off offset:64
	s_waitcnt vmcnt(16)
	s_branch .Lpj_join_1

.Lpj_join_1:
	s_barrier
	s_setprio 1
	s_waitcnt lgkmcnt(1)
	v_mfma_f32_16x16x32_f16 v[86:89], v[130:133], v[154:157], v[86:89]
	v_mfma_f32_16x16x32_f16 v[74:77], v[130:133], v[162:165], v[74:77]
	v_mfma_f32_16x16x32_f16 v[62:65], v[130:133], v[170:173], v[62:65]
	v_mfma_f32_16x16x32_f16 v[50:53], v[130:133], v[178:181], v[50:53]
	s_waitcnt lgkmcnt(0)
	v_mfma_f32_16x16x32_f16 v[86:89], v[142:145], v[158:161], v[86:89]
	v_mfma_f32_16x16x32_f16 v[74:77], v[142:145], v[166:169], v[74:77]
	v_mfma_f32_16x16x32_f16 v[62:65], v[142:145], v[174:177], v[62:65]
	v_mfma_f32_16x16x32_f16 v[50:53], v[142:145], v[182:185], v[50:53]
	s_setprio 0
	s_barrier
	s_mov_b32 m0, s56
	ds_read_b128 v[130:133], v138
	ds_read_b128 v[142:145], v138 offset:1024
	ds_read_b128 v[146:149], v138 offset:2048
	ds_read_b128 v[150:153], v138 offset:3072
	ds_read_b128 v[154:157], v139
	ds_read_b128 v[158:161], v139 offset:1024
	ds_read_b128 v[162:165], v139 offset:2048
	ds_read_b128 v[166:169], v139 offset:3072
	ds_read_b128 v[170:173], v139 offset:4096
	ds_read_b128 v[174:177], v139 offset:5120
	ds_read_b128 v[178:181], v139 offset:6144
	global_load_lds_dwordx4 v110, s[78:79]
	s_mov_b32 m0, s57
	ds_read_b128 v[182:185], v139 offset:7168
	global_load_lds_dwordx4 v114, s[78:79]
	s_barrier
	s_setprio 1
	s_waitcnt lgkmcnt(7)
	v_mfma_f32_16x16x32_f16 v[94:97], v[130:133], v[154:157], v[94:97]
	v_mfma_f32_16x16x32_f16 v[90:93], v[146:149], v[154:157], v[90:93]
	s_waitcnt lgkmcnt(5)
	v_mfma_f32_16x16x32_f16 v[82:85], v[130:133], v[162:165], v[82:85]
	v_mfma_f32_16x16x32_f16 v[78:81], v[146:149], v[162:165], v[78:81]
	s_waitcnt lgkmcnt(3)
	v_mfma_f32_16x16x32_f16 v[70:73], v[130:133], v[170:173], v[70:73]
	v_mfma_f32_16x16x32_f16 v[66:69], v[146:149], v[170:173], v[66:69]
	s_waitcnt lgkmcnt(1)
	v_mfma_f32_16x16x32_f16 v[58:61], v[130:133], v[178:181], v[58:61]
	v_mfma_f32_16x16x32_f16 v[54:57], v[146:149], v[178:181], v[54:57]
	v_mfma_f32_16x16x32_f16 v[94:97], v[142:145], v[158:161], v[94:97]
	v_mfma_f32_16x16x32_f16 v[90:93], v[150:153], v[158:161], v[90:93]
	v_mfma_f32_16x16x32_f16 v[82:85], v[142:145], v[166:169], v[82:85]
	v_mfma_f32_16x16x32_f16 v[78:81], v[150:153], v[166:169], v[78:81]
	v_mfma_f32_16x16x32_f16 v[70:73], v[142:145], v[174:177], v[70:73]
	v_mfma_f32_16x16x32_f16 v[66:69], v[150:153], v[174:177], v[66:69]
	s_waitcnt lgkmcnt(0)
	v_mfma_f32_16x16x32_f16 v[58:61], v[142:145], v[182:185], v[58:61]
	v_mfma_f32_16x16x32_f16 v[54:57], v[150:153], v[182:185], v[54:57]
	s_setprio 0
	s_barrier
	s_mov_b32 m0, s58
	ds_read_b128 v[130:133], v138 offset:4096
	global_load_lds_dwordx4 v112, s[80:81]
	s_add_i32 m0, s58, 0x2000
	ds_read_b128 v[142:145], v138 offset:5120
	global_load_lds_dwordx4 v116, s[80:81]
	s_add_i32 m0, s58, 0x4000
	s_nop 0
	global_load_lds_dwordx4 v118, s[80:81]
	s_cmp_lg_u32 s67, 0
	s_cbranch_scc1 .Lpj_norm_2
	global_load_dwordx4 v[34:37], v[198:199], off offset:128
	global_load_dwordx4 v[38:41], v[200:201], off
	global_load_dwordx4 v[42:45], v[200:201], off offset:64
	global_load_dwordx4 v[46:49], v[200:201], off offset:128
	s_waitcnt vmcnt(13)
	s_branch .Lpj_join_2

.LBB5_55:
	s_mov_b32 m0, s76
	ds_read_b128 v[44:47], v130 offset:16384
	ds_read_b128 v[56:59], v130 offset:17408
	ds_read_b128 v[60:63], v130 offset:18432
	ds_read_b128 v[64:67], v130 offset:19456
	ds_read_b128 v[68:71], v131
	ds_read_b128 v[96:99], v131 offset:1024
	ds_read_b128 v[136:139], v131 offset:2048
	ds_read_b128 v[140:143], v131 offset:3072
	ds_read_b128 v[144:147], v131 offset:4096
	ds_read_b128 v[148:151], v131 offset:5120
	ds_read_b128 v[152:155], v131 offset:6144
	ds_read_b128 v[156:159], v131 offset:7168
	global_load_lds_dwordx4 v112, s[78:79]
	s_add_i32 m0, s76, 0x2000
	s_add_i32 s76, s27, s54
	global_load_lds_dwordx4 v114, s[78:79]
	s_mov_b32 m0, s76
	s_nop 0
	global_load_lds_dwordx4 v116, s[80:81]
	s_add_i32 m0, s76, 0x2000
	s_nop 0
	global_load_lds_dwordx4 v118, s[80:81]
	s_barrier
	s_setprio 1
	s_waitcnt lgkmcnt(7)
	v_mfma_f32_16x16x32_f16 v[92:95], v[44:47], v[68:71], v[92:95]
	v_mfma_f32_16x16x32_f16 v[88:91], v[60:63], v[68:71], v[88:91]
	s_waitcnt lgkmcnt(5)
	v_mfma_f32_16x16x32_f16 v[76:79], v[44:47], v[136:139], v[76:79]
	v_mfma_f32_16x16x32_f16 v[72:75], v[60:63], v[136:139], v[72:75]
	s_waitcnt lgkmcnt(3)
	v_mfma_f32_16x16x32_f16 v[28:31], v[44:47], v[144:147], v[28:31]
	v_mfma_f32_16x16x32_f16 v[24:27], v[60:63], v[144:147], v[24:27]
	s_waitcnt lgkmcnt(1)
	v_mfma_f32_16x16x32_f16 v[12:15], v[44:47], v[152:155], v[12:15]
	v_mfma_f32_16x16x32_f16 v[8:11], v[60:63], v[152:155], v[8:11]
	v_mfma_f32_16x16x32_f16 v[92:95], v[56:59], v[96:99], v[92:95]
	v_mfma_f32_16x16x32_f16 v[88:91], v[64:67], v[96:99], v[88:91]
	v_mfma_f32_16x16x32_f16 v[76:79], v[56:59], v[140:143], v[76:79]
	v_mfma_f32_16x16x32_f16 v[72:75], v[64:67], v[140:143], v[72:75]
	v_mfma_f32_16x16x32_f16 v[28:31], v[56:59], v[148:151], v[28:31]
	v_mfma_f32_16x16x32_f16 v[24:27], v[64:67], v[148:151], v[24:27]
	s_waitcnt lgkmcnt(0)
	v_mfma_f32_16x16x32_f16 v[12:15], v[56:59], v[156:159], v[12:15]
	v_mfma_f32_16x16x32_f16 v[8:11], v[64:67], v[156:159], v[8:11]
	s_setprio 0
	s_barrier
	s_add_i32 s76, s68, s54
	s_mov_b32 m0, s76
	ds_read_b128 v[44:47], v130 offset:32768
	ds_read_b128 v[56:59], v130 offset:33792
	ds_read_b128 v[60:63], v130 offset:34816
	global_load_lds_dwordx4 v120, s[80:81]
	s_add_i32 m0, s76, 0x2000
	ds_read_b128 v[64:67], v130 offset:35840
	global_load_lds_dwordx4 v122, s[80:81]
	s_waitcnt vmcnt(6)
	s_barrier
	s_setprio 1
	s_waitcnt lgkmcnt(3)
	v_mfma_f32_16x16x32_f16 v[84:87], v[44:47], v[68:71], v[84:87]
	v_mfma_f32_16x16x32_f16 v[52:55], v[44:47], v[136:139], v[52:55]
	s_waitcnt lgkmcnt(1)
	v_mfma_f32_16x16x32_f16 v[48:51], v[60:63], v[136:139], v[48:51]
	v_mfma_f32_16x16x32_f16 v[20:23], v[44:47], v[144:147], v[20:23]
	v_mfma_f32_16x16x32_f16 v[16:19], v[60:63], v[144:147], v[16:19]
	v_mfma_f32_16x16x32_f16 v[4:7], v[44:47], v[152:155], v[4:7]
	v_mfma_f32_16x16x32_f16 v[0:3], v[60:63], v[152:155], v[0:3]
	v_mfma_f32_16x16x32_f16 v[84:87], v[56:59], v[96:99], v[84:87]
	v_mfma_f32_16x16x32_f16 v[68:71], v[60:63], v[68:71], v[80:83]
	v_mfma_f32_16x16x32_f16 v[52:55], v[56:59], v[140:143], v[52:55]
	s_waitcnt lgkmcnt(0)
	v_mfma_f32_16x16x32_f16 v[48:51], v[64:67], v[140:143], v[48:51]
	v_mfma_f32_16x16x32_f16 v[20:23], v[56:59], v[148:151], v[20:23]
	v_mfma_f32_16x16x32_f16 v[16:19], v[64:67], v[148:151], v[16:19]
	v_mfma_f32_16x16x32_f16 v[4:7], v[56:59], v[156:159], v[4:7]
	v_mfma_f32_16x16x32_f16 v[0:3], v[64:67], v[156:159], v[0:3]
	v_mfma_f32_16x16x32_f16 v[68:71], v[64:67], v[96:99], v[68:71]
	s_setprio 0
	s_barrier
	s_add_i32 s76, 0, 0x10000
	s_mov_b32 m0, s57
	v_add_u32_e32 v64, s76, v128
	ds_read_b128 v[44:47], v64
	ds_read_b128 v[56:59], v64 offset:1024
	ds_read_b128 v[60:63], v64 offset:2048
	ds_read_b128 v[64:67], v64 offset:3072
	ds_read_b128 v[80:83], v131 offset:49152
	ds_read_b128 v[96:99], v131 offset:50176
	ds_read_b128 v[136:139], v131 offset:51200
	ds_read_b128 v[140:143], v131 offset:52224
	ds_read_b128 v[144:147], v131 offset:53248
	ds_read_b128 v[148:151], v131 offset:54272
	ds_read_b128 v[152:155], v131 offset:55296
	global_load_lds_dwordx4 v100, s[48:49]
	s_mov_b32 m0, s58
	ds_read_b128 v[156:159], v131 offset:56320
	global_load_lds_dwordx4 v104, s[48:49]
	s_mov_b32 m0, s59
	s_nop 0
	global_load_lds_dwordx4 v102, s[46:47]
	s_mov_b32 m0, s60
	s_nop 0
	global_load_lds_dwordx4 v106, s[46:47]
	s_barrier
	s_setprio 1
	s_waitcnt lgkmcnt(7)
	v_mfma_f32_16x16x32_f16 v[92:95], v[44:47], v[80:83], v[92:95]
	v_mfma_f32_16x16x32_f16 v[88:91], v[60:63], v[80:83], v[88:91]
	s_waitcnt lgkmcnt(5)
	v_mfma_f32_16x16x32_f16 v[76:79], v[44:47], v[136:139], v[76:79]
	v_mfma_f32_16x16x32_f16 v[72:75], v[60:63], v[136:139], v[72:75]
	s_waitcnt lgkmcnt(3)
	v_mfma_f32_16x16x32_f16 v[28:31], v[44:47], v[144:147], v[28:31]
	v_mfma_f32_16x16x32_f16 v[24:27], v[60:63], v[144:147], v[24:27]
	s_waitcnt lgkmcnt(1)
	v_mfma_f32_16x16x32_f16 v[12:15], v[44:47], v[152:155], v[12:15]
	v_mfma_f32_16x16x32_f16 v[8:11], v[60:63], v[152:155], v[8:11]
	v_mfma_f32_16x16x32_f16 v[92:95], v[56:59], v[96:99], v[92:95]
	v_mfma_f32_16x16x32_f16 v[88:91], v[64:67], v[96:99], v[88:91]
	v_mfma_f32_16x16x32_f16 v[76:79], v[56:59], v[140:143], v[76:79]
	v_mfma_f32_16x16x32_f16 v[72:75], v[64:67], v[140:143], v[72:75]
	v_mfma_f32_16x16x32_f16 v[28:31], v[56:59], v[148:151], v[28:31]
	v_mfma_f32_16x16x32_f16 v[24:27], v[64:67], v[148:151], v[24:27]
	s_waitcnt lgkmcnt(0)
	v_mfma_f32_16x16x32_f16 v[12:15], v[56:59], v[156:159], v[12:15]
	v_mfma_f32_16x16x32_f16 v[8:11], v[64:67], v[156:159], v[8:11]
	s_setprio 0
	s_barrier
	s_add_i32 s48, 0, 0x14000
	s_add_u32 s46, s46, s10
	s_addc_u32 s47, s47, s11
	s_mov_b32 m0, s61
	v_add_u32_e32 v64, s48, v128
	ds_read_b128 v[44:47], v64
	ds_read_b128 v[56:59], v64 offset:1024
	ds_read_b128 v[60:63], v64 offset:2048
	global_load_lds_dwordx4 v102, s[46:47]
	s_mov_b32 m0, s62
	ds_read_b128 v[64:67], v64 offset:3072
	global_load_lds_dwordx4 v106, s[46:47]
	s_waitcnt vmcnt(6)
	s_barrier
	s_setprio 1
	s_waitcnt lgkmcnt(3)
	v_mfma_f32_16x16x32_f16 v[84:87], v[44:47], v[80:83], v[84:87]
	v_mfma_f32_16x16x32_f16 v[52:55], v[44:47], v[136:139], v[52:55]
	s_waitcnt lgkmcnt(1)
	v_mfma_f32_16x16x32_f16 v[48:51], v[60:63], v[136:139], v[48:51]
	v_mfma_f32_16x16x32_f16 v[20:23], v[44:47], v[144:147], v[20:23]
	v_mfma_f32_16x16x32_f16 v[16:19], v[60:63], v[144:147], v[16:19]
	v_mfma_f32_16x16x32_f16 v[4:7], v[44:47], v[152:155], v[4:7]
	v_mfma_f32_16x16x32_f16 v[0:3], v[60:63], v[152:155], v[0:3]
	v_mfma_f32_16x16x32_f16 v[84:87], v[56:59], v[96:99], v[84:87]
	v_mfma_f32_16x16x32_f16 v[68:71], v[60:63], v[80:83], v[68:71]
	v_mfma_f32_16x16x32_f16 v[52:55], v[56:59], v[140:143], v[52:55]
	s_waitcnt lgkmcnt(0)
	v_mfma_f32_16x16x32_f16 v[48:51], v[64:67], v[140:143], v[48:51]
	v_mfma_f32_16x16x32_f16 v[20:23], v[56:59], v[148:151], v[20:23]
	v_mfma_f32_16x16x32_f16 v[16:19], v[64:67], v[148:151], v[16:19]
	v_mfma_f32_16x16x32_f16 v[4:7], v[56:59], v[156:159], v[4:7]
	v_mfma_f32_16x16x32_f16 v[0:3], v[64:67], v[156:159], v[0:3]
	v_mfma_f32_16x16x32_f16 v[68:71], v[64:67], v[96:99], v[68:71]
	s_setprio 0
	s_barrier
	s_mov_b32 m0, s64
	ds_read_b128 v[44:47], v132
	ds_read_b128 v[56:59], v132 offset:1024
	ds_read_b128 v[60:63], v132 offset:2048
	ds_read_b128 v[64:67], v132 offset:3072
	ds_read_b128 v[80:83], v133
	ds_read_b128 v[96:99], v133 offset:1024
	ds_read_b128 v[136:139], v133 offset:2048
	ds_read_b128 v[140:143], v133 offset:3072
	ds_read_b128 v[144:147], v133 offset:4096
	ds_read_b128 v[148:151], v133 offset:5120
	ds_read_b128 v[152:155], v133 offset:6144
	ds_read_b128 v[156:159], v133 offset:7168
	global_load_lds_dwordx4 v100, s[82:83]
	s_mov_b32 m0, s65
	s_add_i32 s46, s76, s54
	global_load_lds_dwordx4 v104, s[82:83]
	s_mov_b32 m0, s46
	s_nop 0
	global_load_lds_dwordx4 v102, s[84:85]
	s_add_i32 m0, s46, 0x2000
	s_nop 0
	global_load_lds_dwordx4 v106, s[84:85]
	s_barrier
	s_setprio 1
	s_waitcnt lgkmcnt(7)
	v_mfma_f32_16x16x32_f16 v[92:95], v[44:47], v[80:83], v[92:95]
	v_mfma_f32_16x16x32_f16 v[88:91], v[60:63], v[80:83], v[88:91]
	s_waitcnt lgkmcnt(5)
	v_mfma_f32_16x16x32_f16 v[76:79], v[44:47], v[136:139], v[76:79]
	v_mfma_f32_16x16x32_f16 v[72:75], v[60:63], v[136:139], v[72:75]
	s_waitcnt lgkmcnt(3)
	v_mfma_f32_16x16x32_f16 v[28:31], v[44:47], v[144:147], v[28:31]
	v_mfma_f32_16x16x32_f16 v[24:27], v[60:63], v[144:147], v[24:27]
	s_waitcnt lgkmcnt(1)
	v_mfma_f32_16x16x32_f16 v[12:15], v[44:47], v[152:155], v[12:15]
	v_mfma_f32_16x16x32_f16 v[8:11], v[60:63], v[152:155], v[8:11]
	v_mfma_f32_16x16x32_f16 v[92:95], v[56:59], v[96:99], v[92:95]
	v_mfma_f32_16x16x32_f16 v[88:91], v[64:67], v[96:99], v[88:91]
	v_mfma_f32_16x16x32_f16 v[76:79], v[56:59], v[140:143], v[76:79]
	v_mfma_f32_16x16x32_f16 v[72:75], v[64:67], v[140:143], v[72:75]
	v_mfma_f32_16x16x32_f16 v[28:31], v[56:59], v[148:151], v[28:31]
	v_mfma_f32_16x16x32_f16 v[24:27], v[64:67], v[148:151], v[24:27]
	s_waitcnt lgkmcnt(0)
	v_mfma_f32_16x16x32_f16 v[12:15], v[56:59], v[156:159], v[12:15]
	v_mfma_f32_16x16x32_f16 v[8:11], v[64:67], v[156:159], v[8:11]
	s_setprio 0
	s_barrier
	s_add_i32 s46, s48, s54
	s_mov_b32 m0, s46
	ds_read_b128 v[44:47], v134
	ds_read_b128 v[56:59], v134 offset:1024
	ds_read_b128 v[60:63], v134 offset:2048
	global_load_lds_dwordx4 v102, s[86:87]
	s_add_i32 m0, s46, 0x2000
	ds_read_b128 v[64:67], v134 offset:3072
	global_load_lds_dwordx4 v106, s[86:87]
	s_waitcnt vmcnt(6)
	s_barrier
	s_setprio 1
	s_waitcnt lgkmcnt(3)
	v_mfma_f32_16x16x32_f16 v[84:87], v[44:47], v[80:83], v[84:87]
	s_waitcnt lgkmcnt(1)
	v_mfma_f32_16x16x32_f16 v[68:71], v[60:63], v[80:83], v[68:71]
	v_mfma_f32_16x16x32_f16 v[52:55], v[44:47], v[136:139], v[52:55]
	v_mfma_f32_16x16x32_f16 v[48:51], v[60:63], v[136:139], v[48:51]
	v_mfma_f32_16x16x32_f16 v[20:23], v[44:47], v[144:147], v[20:23]
	v_mfma_f32_16x16x32_f16 v[16:19], v[60:63], v[144:147], v[16:19]
	v_mfma_f32_16x16x32_f16 v[4:7], v[44:47], v[152:155], v[4:7]
	v_mfma_f32_16x16x32_f16 v[0:3], v[60:63], v[152:155], v[0:3]
	v_mfma_f32_16x16x32_f16 v[84:87], v[56:59], v[96:99], v[84:87]
	s_waitcnt lgkmcnt(0)
	v_mfma_f32_16x16x32_f16 v[80:83], v[64:67], v[96:99], v[68:71]
	v_mfma_f32_16x16x32_f16 v[52:55], v[56:59], v[140:143], v[52:55]
	v_mfma_f32_16x16x32_f16 v[48:51], v[64:67], v[140:143], v[48:51]
	v_mfma_f32_16x16x32_f16 v[20:23], v[56:59], v[148:151], v[20:23]
	v_mfma_f32_16x16x32_f16 v[16:19], v[64:67], v[148:151], v[16:19]
	v_mfma_f32_16x16x32_f16 v[4:7], v[56:59], v[156:159], v[4:7]
	v_mfma_f32_16x16x32_f16 v[0:3], v[64:67], v[156:159], v[0:3]
	s_setprio 0
	s_add_i32 s75, s75, 3
	s_add_u32 s44, s44, 0x180
	s_addc_u32 s45, s45, 0
	s_cmp_ge_i32 s75, s66
	s_cbranch_scc1 .Lrot_exit_mlp1
	s_add_u32 s78, s40, s44
	s_addc_u32 s79, s41, s45
	s_add_u32 s80, s42, s44
	s_addc_u32 s81, s43, s45
	s_add_u32 s46, s40, s44
	s_addc_u32 s47, s41, s45
	s_add_u32 s46, s46, 0x180
	s_addc_u32 s47, s47, 0
	s_add_u32 s48, s42, s44
	s_addc_u32 s49, s43, s45
	s_add_u32 s76, s48, 0x180
	s_addc_u32 s77, s49, 0
	s_cmp_eq_u32 s67, s75
	s_cselect_b32 s49, s7, s47
	s_cselect_b32 s48, s6, s46
	s_cselect_b32 s47, s5, s77
	s_cselect_b32 s46, s4, s76
	s_add_u32 s82, s48, 0x80
	s_addc_u32 s83, s49, 0
	s_add_u32 s84, s46, 0x80
	s_addc_u32 s85, s47, 0
	s_add_u32 s86, s84, s10
	s_addc_u32 s87, s85, s11
	s_add_i32 s76, s19, s54
	s_barrier
	s_branch .LBB5_55

.LBB6_22:
	s_mov_b32 m0, s68
	ds_read_b128 v[132:135], v131 offset:16384
	ds_read_b128 v[136:139], v131 offset:17408
	ds_read_b128 v[140:143], v131 offset:18432
	ds_read_b128 v[144:147], v131 offset:19456
	ds_read_b128 v[148:151], v182
	ds_read_b128 v[152:155], v182 offset:1024
	ds_read_b128 v[156:159], v182 offset:2048
	ds_read_b128 v[160:163], v182 offset:3072
	ds_read_b128 v[164:167], v182 offset:4096
	ds_read_b128 v[168:171], v182 offset:5120
	ds_read_b128 v[172:175], v182 offset:6144
	global_load_lds_dwordx4 v106, s[72:73]
	s_add_i32 m0, s68, 0x2000
	ds_read_b128 v[176:179], v182 offset:7168
	global_load_lds_dwordx4 v108, s[72:73]
	s_barrier
	s_setprio 1
	s_waitcnt lgkmcnt(7)
	v_mfma_f32_16x16x32_f16 v[40:43], v[132:135], v[148:151], v[40:43]
	v_mfma_f32_16x16x32_f16 v[44:47], v[140:143], v[148:151], v[44:47]
	s_waitcnt lgkmcnt(5)
	v_mfma_f32_16x16x32_f16 v[32:35], v[132:135], v[156:159], v[32:35]
	v_mfma_f32_16x16x32_f16 v[28:31], v[140:143], v[156:159], v[28:31]
	s_waitcnt lgkmcnt(3)
	v_mfma_f32_16x16x32_f16 v[20:23], v[132:135], v[164:167], v[20:23]
	v_mfma_f32_16x16x32_f16 v[16:19], v[140:143], v[164:167], v[16:19]
	s_waitcnt lgkmcnt(1)
	v_mfma_f32_16x16x32_f16 v[8:11], v[132:135], v[172:175], v[8:11]
	v_mfma_f32_16x16x32_f16 v[4:7], v[140:143], v[172:175], v[4:7]
	v_mfma_f32_16x16x32_f16 v[40:43], v[136:139], v[152:155], v[40:43]
	v_mfma_f32_16x16x32_f16 v[44:47], v[144:147], v[152:155], v[44:47]
	v_mfma_f32_16x16x32_f16 v[32:35], v[136:139], v[160:163], v[32:35]
	v_mfma_f32_16x16x32_f16 v[28:31], v[144:147], v[160:163], v[28:31]
	v_mfma_f32_16x16x32_f16 v[20:23], v[136:139], v[168:171], v[20:23]
	v_mfma_f32_16x16x32_f16 v[16:19], v[144:147], v[168:171], v[16:19]
	s_waitcnt lgkmcnt(0)
	v_mfma_f32_16x16x32_f16 v[8:11], v[136:139], v[176:179], v[8:11]
	v_mfma_f32_16x16x32_f16 v[4:7], v[144:147], v[176:179], v[4:7]
	s_setprio 0
	s_barrier
	s_add_i32 m0, s47, 0x18000
	ds_read_b128 v[132:135], v131 offset:20480
	global_load_lds_dwordx4 v110, s[74:75]
	s_add_i32 m0, s47, 0x1a000
	ds_read_b128 v[136:139], v131 offset:21504
	global_load_lds_dwordx4 v112, s[74:75]
	s_add_i32 m0, s47, 0x1c000
	s_nop 0
	global_load_lds_dwordx4 v114, s[74:75]
	s_cmp_lg_u32 s65, 0
	s_cbranch_scc1 .Lm2_norm_0
	s_mul_i32 s70, s58, 0xc0
	v_add_u32_e32 v234, s70, v129
	v_ashrrev_i32_e32 v235, 31, v234
	v_lshlrev_b64 v[234:235], 2, v[234:235]
	v_lshl_add_u64 v[234:235], s[18:19], 0, v[234:235]
	global_load_dwordx4 v[222:225], v[234:235], off
	global_load_dwordx4 v[226:229], v[234:235], off offset:64
	global_load_dwordx4 v[230:233], v[234:235], off offset:128
	global_load_dwordx2 v[198:199], v[190:191], off
	global_load_dwordx2 v[200:201], v[190:191], off offset:32
	global_load_dwordx2 v[202:203], v[190:191], off offset:64
	global_load_dwordx2 v[204:205], v[192:193], off
	s_waitcnt vmcnt(12)
	s_branch .Lm2_join_0

.Lm2_join_0:
	s_barrier
	s_setprio 1
	s_waitcnt lgkmcnt(1)
	v_mfma_f32_16x16x32_f16 v[36:39], v[132:135], v[148:151], v[36:39]
	v_mfma_f32_16x16x32_f16 v[24:27], v[132:135], v[156:159], v[24:27]
	v_mfma_f32_16x16x32_f16 v[12:15], v[132:135], v[164:167], v[12:15]
	v_mfma_f32_16x16x32_f16 v[0:3], v[132:135], v[172:175], v[0:3]
	s_waitcnt lgkmcnt(0)
	v_mfma_f32_16x16x32_f16 v[36:39], v[136:139], v[152:155], v[36:39]
	v_mfma_f32_16x16x32_f16 v[24:27], v[136:139], v[160:163], v[24:27]
	v_mfma_f32_16x16x32_f16 v[12:15], v[136:139], v[168:171], v[12:15]
	v_mfma_f32_16x16x32_f16 v[0:3], v[136:139], v[176:179], v[0:3]
	s_setprio 0
	s_barrier
	s_mov_b32 m0, s47
	ds_read_b128 v[132:135], v131 offset:57344
	ds_read_b128 v[136:139], v131 offset:58368
	ds_read_b128 v[140:143], v131 offset:59392
	ds_read_b128 v[144:147], v131 offset:60416
	ds_read_b128 v[148:151], v182 offset:40960
	ds_read_b128 v[152:155], v182 offset:41984
	ds_read_b128 v[156:159], v182 offset:43008
	ds_read_b128 v[160:163], v182 offset:44032
	ds_read_b128 v[164:167], v182 offset:45056
	ds_read_b128 v[168:171], v182 offset:46080
	ds_read_b128 v[172:175], v182 offset:47104
	global_load_lds_dwordx4 v48, s[66:67]
	s_mov_b32 m0, s48
	ds_read_b128 v[176:179], v182 offset:48128
	global_load_lds_dwordx4 v52, s[66:67]
	s_barrier
	s_setprio 1
	s_waitcnt lgkmcnt(7)
	v_mfma_f32_16x16x32_f16 v[40:43], v[132:135], v[148:151], v[40:43]
	v_mfma_f32_16x16x32_f16 v[44:47], v[140:143], v[148:151], v[44:47]
	s_waitcnt lgkmcnt(5)
	v_mfma_f32_16x16x32_f16 v[32:35], v[132:135], v[156:159], v[32:35]
	v_mfma_f32_16x16x32_f16 v[28:31], v[140:143], v[156:159], v[28:31]
	s_waitcnt lgkmcnt(3)
	v_mfma_f32_16x16x32_f16 v[20:23], v[132:135], v[164:167], v[20:23]
	v_mfma_f32_16x16x32_f16 v[16:19], v[140:143], v[164:167], v[16:19]
	s_waitcnt lgkmcnt(1)
	v_mfma_f32_16x16x32_f16 v[8:11], v[132:135], v[172:175], v[8:11]
	v_mfma_f32_16x16x32_f16 v[4:7], v[140:143], v[172:175], v[4:7]
	v_mfma_f32_16x16x32_f16 v[40:43], v[136:139], v[152:155], v[40:43]
	v_mfma_f32_16x16x32_f16 v[44:47], v[144:147], v[152:155], v[44:47]
	v_mfma_f32_16x16x32_f16 v[32:35], v[136:139], v[160:163], v[32:35]
	v_mfma_f32_16x16x32_f16 v[28:31], v[144:147], v[160:163], v[28:31]
	v_mfma_f32_16x16x32_f16 v[20:23], v[136:139], v[168:171], v[20:23]
	v_mfma_f32_16x16x32_f16 v[16:19], v[144:147], v[168:171], v[16:19]
	s_waitcnt lgkmcnt(0)
	v_mfma_f32_16x16x32_f16 v[8:11], v[136:139], v[176:179], v[8:11]
	v_mfma_f32_16x16x32_f16 v[4:7], v[144:147], v[176:179], v[4:7]
	s_setprio 0
	s_barrier
	s_mov_b32 m0, s49
	ds_read_b128 v[132:135], v131 offset:61440
	global_load_lds_dwordx4 v50, s[30:31]
	s_mov_b32 m0, s50
	ds_read_b128 v[136:139], v131 offset:62464
	global_load_lds_dwordx4 v54, s[30:31]
	s_mov_b32 m0, s51
	s_nop 0
	global_load_lds_dwordx4 v56, s[30:31]
	s_cmp_lg_u32 s65, 0
	s_cbranch_scc1 .Lm2_norm_1
	global_load_dwordx2 v[206:207], v[192:193], off offset:32
	global_load_dwordx2 v[208:209], v[192:193], off offset:64
	global_load_dwordx2 v[210:211], v[194:195], off
	global_load_dwordx2 v[212:213], v[194:195], off offset:32
	s_waitcnt vmcnt(16)
	s_branch .Lm2_join_1

.Lm2_join_1:
	s_barrier
	s_setprio 1
	s_waitcnt lgkmcnt(1)
	v_mfma_f32_16x16x32_f16 v[36:39], v[132:135], v[148:151], v[36:39]
	v_mfma_f32_16x16x32_f16 v[24:27], v[132:135], v[156:159], v[24:27]
	v_mfma_f32_16x16x32_f16 v[12:15], v[132:135], v[164:167], v[12:15]
	v_mfma_f32_16x16x32_f16 v[0:3], v[132:135], v[172:175], v[0:3]
	s_waitcnt lgkmcnt(0)
	v_mfma_f32_16x16x32_f16 v[36:39], v[136:139], v[152:155], v[36:39]
	v_mfma_f32_16x16x32_f16 v[24:27], v[136:139], v[160:163], v[24:27]
	v_mfma_f32_16x16x32_f16 v[12:15], v[136:139], v[168:171], v[12:15]
	v_mfma_f32_16x16x32_f16 v[0:3], v[136:139], v[176:179], v[0:3]
	s_setprio 0
	s_barrier
	s_mov_b32 m0, s54
	v_add_u32_e32 v131, s62, v127
	ds_read_b128 v[132:135], v130
	ds_read_b128 v[136:139], v130 offset:1024
	ds_read_b128 v[140:143], v130 offset:2048
	ds_read_b128 v[144:147], v130 offset:3072
	ds_read_b128 v[148:151], v131
	ds_read_b128 v[152:155], v131 offset:1024
	ds_read_b128 v[156:159], v131 offset:2048
	ds_read_b128 v[160:163], v131 offset:3072
	ds_read_b128 v[164:167], v131 offset:4096
	ds_read_b128 v[168:171], v131 offset:5120
	ds_read_b128 v[172:175], v131 offset:6144
	global_load_lds_dwordx4 v48, s[76:77]
	s_mov_b32 m0, s55
	ds_read_b128 v[176:179], v131 offset:7168
	global_load_lds_dwordx4 v52, s[76:77]
	s_barrier
	s_setprio 1
	s_waitcnt lgkmcnt(7)
	v_mfma_f32_16x16x32_f16 v[40:43], v[132:135], v[148:151], v[40:43]
	v_mfma_f32_16x16x32_f16 v[44:47], v[140:143], v[148:151], v[44:47]
	s_waitcnt lgkmcnt(5)
	v_mfma_f32_16x16x32_f16 v[32:35], v[132:135], v[156:159], v[32:35]
	v_mfma_f32_16x16x32_f16 v[28:31], v[140:143], v[156:159], v[28:31]
	s_waitcnt lgkmcnt(3)
	v_mfma_f32_16x16x32_f16 v[20:23], v[132:135], v[164:167], v[20:23]
	v_mfma_f32_16x16x32_f16 v[16:19], v[140:143], v[164:167], v[16:19]
	s_waitcnt lgkmcnt(1)
	v_mfma_f32_16x16x32_f16 v[8:11], v[132:135], v[172:175], v[8:11]
	v_mfma_f32_16x16x32_f16 v[4:7], v[140:143], v[172:175], v[4:7]
	v_mfma_f32_16x16x32_f16 v[40:43], v[136:139], v[152:155], v[40:43]
	v_mfma_f32_16x16x32_f16 v[44:47], v[144:147], v[152:155], v[44:47]
	v_mfma_f32_16x16x32_f16 v[32:35], v[136:139], v[160:163], v[32:35]
	v_mfma_f32_16x16x32_f16 v[28:31], v[144:147], v[160:163], v[28:31]
	v_mfma_f32_16x16x32_f16 v[20:23], v[136:139], v[168:171], v[20:23]
	v_mfma_f32_16x16x32_f16 v[16:19], v[144:147], v[168:171], v[16:19]
	s_waitcnt lgkmcnt(0)
	v_mfma_f32_16x16x32_f16 v[8:11], v[136:139], v[176:179], v[8:11]
	v_mfma_f32_16x16x32_f16 v[4:7], v[144:147], v[176:179], v[4:7]
	s_setprio 0
	s_barrier
	s_mov_b32 m0, s56
	ds_read_b128 v[132:135], v130 offset:4096
	global_load_lds_dwordx4 v50, s[78:79]
	s_add_i32 m0, s56, 0x2000
	ds_read_b128 v[136:139], v130 offset:5120
	global_load_lds_dwordx4 v54, s[78:79]
	s_add_i32 m0, s56, 0x4000
	s_nop 0
	global_load_lds_dwordx4 v56, s[78:79]
	s_cmp_lg_u32 s65, 0
	s_cbranch_scc1 .Lm2_norm_2
	global_load_dwordx2 v[214:215], v[194:195], off offset:64
	global_load_dwordx2 v[216:217], v[196:197], off
	global_load_dwordx2 v[218:219], v[196:197], off offset:32
	global_load_dwordx2 v[220:221], v[196:197], off offset:64
	s_waitcnt vmcnt(13)
	s_branch .Lm2_join_2
